# attention first half-step: the 16 row-sum v_add_f32 of the previous tile moved in front of the first QK^T MFMA (into the LDS-read wait) instead of being spread over the first four MFMAs
# speedup vs baseline: 1.0016x; 1.0016x over previous
; __device__ __forceinline__ unsigned sel_bit_mask(unsigned w, int b) { unsigned m; asm("v_bfe_i32 %0, %1, %2, 1" : "=v"(m) : "v"(w), "n"(b)); return m; }
; template <bool SEL>
; __device__ __forceinline__ void finishSM(f32x16& p0, f32x16& p1, float alpha, float& l_reg, bf16x8& pa0, bf16x8& pa1, bf16x8& pa2, bf16x8& pa3, unsigned selw) {
; #pragma unroll
;     for (int r = 0; r < 16; ++r) p1[r] = __builtin_amdgcn_exp2f(p1[r]);
;     if (SEL) {
; #pragma unroll
;         for (int r = 0; r < 16; ++r) p1[r] = __uint_as_float(__float_as_uint(p1[r]) & sel_bit_mask(selw, 16 + r));
;     }
;     float ps = 0;
; #pragma unroll
;     for (int r = 0; r < 16; ++r) ps += p0[r];
; #pragma unroll
;     for (int r = 0; r < 16; ++r) ps += p1[r];
;     { auto rr = __builtin_amdgcn_permlane32_swap(__float_as_uint(ps), __float_as_uint(ps), false, false);
;       ps = __uint_as_float(rr[0]) + __uint_as_float(rr[1]); }
;     l_reg = l_reg * alpha + ps;
;     ...
;     PK4(p0, 0, pa0); PK4(p0, 8, pa1); PK4(p1, 0, pa2); PK4(p1, 8, pa3);
;     ...
; }
; template <int KB, int QREG>
; __device__ __forceinline__ void qkt(f32x16& p0, f32x16& p1, const char* K_lds, int r32, int hi, const bf16x8* qr, const char* qlds) {
;     p0 = f32x16{}; p1 = f32x16{};
;     const char* kb[4];
; #pragma unroll
;     for (int dd = 0; dd < 4; ++dd) kb[dd] = K_lds + KB * SHM_K + KSWZ(r32, (dd * 16 + hi * 8) * 2);
; #pragma unroll
;     for (int d0 = 0; d0 < 8; ++d0) { const char* a = kb[d0 & 3] + (d0 >> 2) * 128;
;         bf16x8 b0 = *reinterpret_cast<const bf16x8*>(a);
;         bf16x8 b1 = *reinterpret_cast<const bf16x8*>(a + 32 * 256);
;         const bf16x8 qf = (d0 < QREG) ? qr[d0 < QREG ? d0 : 0] : *reinterpret_cast<const bf16x8*>(qlds + (d0 - QREG) * 1024);
;         p0 = __builtin_amdgcn_mfma_f32_32x32x16_bf16(b0, qf, p0, 0, 0, 0);
;         p1 = __builtin_amdgcn_mfma_f32_32x32x16_bf16(b1, qf, p1, 0, 0, 0); }
; }
.LBB0_1812:
	ds_read_b128 v[2:5], v213 offset:49152
	ds_read_b128 v[250:253], v212 offset:49152
	ds_read_b128 v[6:9], v213 offset:49280
	v_add_f32_e32 v0, 0, v126
	v_add_f32_e32 v0, v127, v0
	v_add_f32_e32 v0, v124, v0
	v_add_f32_e32 v0, v125, v0
	v_add_f32_e32 v0, v122, v0
	v_add_f32_e32 v0, v123, v0
	v_add_f32_e32 v0, v120, v0
	v_add_f32_e32 v0, v121, v0
	v_add_f32_e32 v0, v118, v0
	v_add_f32_e32 v0, v119, v0
	v_add_f32_e32 v0, v116, v0
	v_add_f32_e32 v0, v117, v0
	v_add_f32_e32 v0, v114, v0
	v_add_f32_e32 v0, v115, v0
	v_add_f32_e32 v0, v112, v0
	v_add_f32_e32 v0, v113, v0
	s_waitcnt lgkmcnt(2)
	v_mfma_f32_32x32x16_bf16 v[96:111], v[2:5], v[164:167], 0
	ds_read_b128 v[2:5], v213 offset:57344
	ds_read_b128 v[10:13], v212 offset:49280
	s_waitcnt lgkmcnt(3)
	v_mfma_f32_32x32x16_bf16 v[96:111], v[250:253], v[160:163], v[96:111]
	ds_read_b128 v[250:253], v212 offset:57344
	ds_read_b128 v[128:131], v213 offset:57472
	s_waitcnt lgkmcnt(3)
	v_mfma_f32_32x32x16_bf16 v[80:95], v[2:5], v[164:167], 0
	ds_read_b128 v[2:5], v211 offset:49152
	ds_read_b128 v[132:135], v212 offset:57472
	s_waitcnt lgkmcnt(3)
	v_mfma_f32_32x32x16_bf16 v[80:95], v[250:253], v[160:163], v[80:95]
	ds_read_b128 v[250:253], v211 offset:57344
	ds_read_b128 v[136:139], v211 offset:49280
	s_waitcnt lgkmcnt(3)
	v_mfma_f32_32x32x16_bf16 v[96:111], v[2:5], v[156:159], v[96:111]
	ds_read_b128 v[2:5], v210 offset:49152
	ds_read_b128 v[140:143], v211 offset:57472
	s_waitcnt lgkmcnt(3)
	v_mfma_f32_32x32x16_bf16 v[80:95], v[250:253], v[156:159], v[80:95]
	ds_read_b128 v[250:253], v210 offset:57344
	ds_read_b128 v[220:223], v210 offset:49280
	s_waitcnt lgkmcnt(3)
	v_mfma_f32_32x32x16_bf16 v[96:111], v[2:5], v[152:155], v[96:111]
	ds_read_b128 v[224:227], v210 offset:57472
	s_waitcnt lgkmcnt(2)
	v_mfma_f32_32x32x16_bf16 v[80:95], v[250:253], v[152:155], v[80:95]
	v_mfma_f32_32x32x16_bf16 v[96:111], v[6:9], v[148:151], v[96:111]
	ds_read_b128 v[2:5], v208
	ds_read_b128 v[6:9], v208 offset:1024
	v_cvt_pk_bf16_f32 v126, v126, v127
	v_cvt_pk_bf16_f32 v127, v124, v125
	v_exp_f32_e32 v124, v172
	v_exp_f32_e32 v125, v173
	v_mfma_f32_32x32x16_bf16 v[80:95], v[128:131], v[148:151], v[80:95]
	v_cvt_pk_bf16_f32 v128, v122, v123
	v_exp_f32_e32 v122, v174
	v_exp_f32_e32 v123, v175
	v_exp_f32_e32 v129, v170
	v_exp_f32_e32 v130, v171
	v_exp_f32_e32 v131, v168
	v_permlane32_swap_b32_e32 v126, v128
	v_mfma_f32_32x32x16_bf16 v[96:111], v[10:13], v[144:147], v[96:111]
	v_exp_f32_e32 v10, v178
	v_exp_f32_e32 v11, v179
	v_exp_f32_e32 v12, v176
	v_exp_f32_e32 v13, v177
	v_mfma_f32_32x32x16_bf16 v[80:95], v[132:135], v[144:147], v[80:95]
	v_bfe_i32 v133, v195, 16, 1
	v_exp_f32_e32 v132, v169
	s_waitcnt lgkmcnt(1)
	v_mfma_f32_32x32x16_bf16 v[96:111], v[136:139], v[2:5], v[96:111]
	v_mfma_f32_32x32x16_bf16 v[80:95], v[140:143], v[2:5], v[80:95]
	v_exp_f32_e32 v2, v182
	v_exp_f32_e32 v3, v183
	v_exp_f32_e32 v4, v180
	v_exp_f32_e32 v5, v181
	v_and_b32_e32 v2, v133, v2
	v_bfe_i32 v133, v195, 17, 1
	v_add_f32_e32 v0, v0, v2
	v_and_b32_e32 v3, v133, v3
	v_bfe_i32 v133, v195, 18, 1
	v_add_f32_e32 v0, v0, v3
	v_and_b32_e32 v4, v133, v4
	v_bfe_i32 v133, v195, 19, 1
	v_add_f32_e32 v0, v0, v4
	v_and_b32_e32 v5, v133, v5
	v_bfe_i32 v133, v195, 20, 1
	v_add_f32_e32 v0, v0, v5
	v_and_b32_e32 v10, v133, v10
	v_bfe_i32 v133, v195, 21, 1
	v_add_f32_e32 v0, v0, v10
	v_and_b32_e32 v11, v133, v11
	v_bfe_i32 v133, v195, 22, 1
	v_add_f32_e32 v0, v0, v11
	v_and_b32_e32 v12, v133, v12
	v_bfe_i32 v133, v195, 23, 1
	v_add_f32_e32 v0, v0, v12
	v_and_b32_e32 v13, v133, v13
	v_bfe_i32 v133, v195, 24, 1
	v_add_f32_e32 v0, v0, v13
	v_and_b32_e32 v122, v133, v122
	v_bfe_i32 v133, v195, 25, 1
	v_add_f32_e32 v0, v0, v122
	v_and_b32_e32 v123, v133, v123
	v_bfe_i32 v133, v195, 26, 1
	v_add_f32_e32 v0, v0, v123
	v_and_b32_e32 v124, v133, v124
	v_bfe_i32 v133, v195, 27, 1
	s_waitcnt lgkmcnt(0)
	v_mfma_f32_32x32x16_bf16 v[96:111], v[220:223], v[6:9], v[96:111]
	v_and_b32_e32 v125, v133, v125
	v_bfe_i32 v133, v195, 28, 1
	v_add_f32_e32 v0, v0, v124
	v_and_b32_e32 v133, v133, v129
	v_add_f32_e32 v0, v0, v125
	v_bfe_i32 v129, v195, 29, 1
	v_add_f32_e32 v0, v0, v133
	v_mfma_f32_32x32x16_bf16 v[80:95], v[224:227], v[6:9], v[80:95]
	ds_read_b64_tr_b16 v[242:243], v206 offset:0
	ds_read_b64_tr_b16 v[244:245], v206 offset:0x800
	ds_read_b64_tr_b16 v[134:135], v206 offset:0x1000
	ds_read_b64_tr_b16 v[136:137], v206 offset:0x1800
	ds_read_b64_tr_b16 v[138:139], v206 offset:0x2000
	ds_read_b64_tr_b16 v[140:141], v206 offset:0x2800
	ds_read_b64_tr_b16 v[172:173], v206 offset:0x3000
	ds_read_b64_tr_b16 v[174:175], v206 offset:0x3800
	v_and_b32_e32 v130, v129, v130
	v_bfe_i32 v129, v195, 30, 1
	v_add_f32_e32 v0, v0, v130
	v_and_b32_e32 v131, v129, v131
	v_bfe_i32 v129, v195, 31, 1
	v_add_f32_e32 v0, v0, v131
	v_and_b32_e32 v132, v129, v132
	v_add_f32_e32 v189, v0, v132
	v_mov_b32_e32 v219, v189
	v_cvt_pk_bf16_f32 v129, v120, v121
	v_cvt_pk_bf16_f32 v118, v118, v119
	v_cvt_pk_bf16_f32 v119, v116, v117
	v_cvt_pk_bf16_f32 v120, v114, v115
	v_cvt_pk_bf16_f32 v121, v112, v113
	v_cvt_pk_bf16_f32 v112, v2, v3
	v_cvt_pk_bf16_f32 v113, v4, v5
	v_cvt_pk_bf16_f32 v114, v10, v11
	v_cvt_pk_bf16_f32 v115, v12, v13
	v_cvt_pk_bf16_f32 v122, v122, v123
	v_cvt_pk_bf16_f32 v123, v124, v125
	v_cvt_pk_bf16_f32 v124, v133, v130
	v_cvt_pk_bf16_f32 v125, v131, v132
	s_nop 1
	v_permlane32_swap_b32_e32 v189, v219
	v_permlane32_swap_b32_e32 v127, v129
	v_permlane32_swap_b32_e32 v118, v120
	v_permlane32_swap_b32_e32 v119, v121
	v_permlane32_swap_b32_e32 v112, v114
	v_permlane32_swap_b32_e32 v113, v115
	v_permlane32_swap_b32_e32 v122, v124
	v_permlane32_swap_b32_e32 v123, v125
	v_add_u32_e32 v4, 32, v196
	v_add_u32_e32 v0, -2, v194
	v_ashrrev_i32_e32 v197, 31, v196
	v_ashrrev_i32_e32 v5, 31, v4
	v_lshl_add_u64 v[2:3], v[0:1], 2, s[44:45]
	v_lshlrev_b64 v[10:11], 10, v[196:197]
	v_lshlrev_b64 v[12:13], 10, v[4:5]
	global_load_dword v217, v[2:3], off
	v_lshl_add_u64 v[2:3], v[14:15], 0, v[10:11]
	v_lshl_add_u64 v[6:7], v[14:15], 0, v[12:13]
	v_lshl_add_u64 v[10:11], v[192:193], 0, v[10:11]
	global_load_dwordx4 v[2:5], v[2:3], off
	s_nop 0
	global_load_dwordx4 v[6:9], v[6:7], off
	v_lshl_add_u64 v[116:117], v[192:193], 0, v[12:13]
	global_load_dwordx4 v[10:13], v[10:11], off
	s_nop 0
	global_load_dwordx4 v[168:171], v[116:117], off
	s_nop 0
	s_waitcnt lgkmcnt(6)
; __device__ __forceinline__ unsigned sel_bit_mask(unsigned w, int b) { unsigned m; asm("v_bfe_i32 %0, %1, %2, 1" : "=v"(m) : "v"(w), "n"(b)); return m; }
; template <bool SEL>
; __device__ __forceinline__ void partialSM(f32x16& p0, f32x16& p1, float& m_reg, float& mn, float& alpha, unsigned selw) {
;     float pmax = p0[0];
; #pragma unroll
;     for (int r = 1; r < 16; ++r) pmax = fmaxf(pmax, p0[r]);
; #pragma unroll
;     for (int r = 0; r < 16; ++r) pmax = fmaxf(pmax, p1[r]);
;     { auto rr = __builtin_amdgcn_permlane32_swap(__float_as_uint(pmax), __float_as_uint(pmax), false, false);
;       pmax = fmaxf(__uint_as_float(rr[0]), __uint_as_float(rr[1])); }
;     constexpr float C2 = 1.4426950408889634f * SCALE;
;     if (__builtin_expect(__all((pmax - m_reg) * SCALE <= THR), 1)) { mn = m_reg; alpha = 1.f; }
;     else { mn = fmaxf(m_reg, pmax); alpha = __builtin_amdgcn_exp2f((m_reg - mn) * C2); m_reg = mn; }
;     const float mnL = -mn * C2;
; #pragma unroll
;     for (int r = 0; r < 16; ++r) p0[r] = fmaf(p0[r], C2, mnL);
; #pragma unroll
;     for (int r = 0; r < 16; ++r) p1[r] = fmaf(p1[r], C2, mnL);
; #pragma unroll
;     for (int r = 0; r < 16; ++r) p0[r] = __builtin_amdgcn_exp2f(p0[r]);
;     if (SEL) {
; #pragma unroll
;         for (int r = 0; r < 16; ++r) p0[r] = __uint_as_float(__float_as_uint(p0[r]) & sel_bit_mask(selw, r));
;     }
; }
; template <int VB>
; __device__ __forceinline__ void pv_tile(f32x16* o, int vb0, bf16x8 pa0, bf16x8 pa1, bf16x8 pa2, bf16x8 pa3) {
;     ...
;     PV_D0(0); PV_D0(1); PV_D0(2); PV_D0(3);
;     ...
; }
	v_mfma_f32_32x32x16_bf16 v[64:79], v[126:129], v[242:245], v[64:79]
	ds_read_b64_tr_b16 v[130:131], v206 offset:0x200
	ds_read_b64_tr_b16 v[132:133], v206 offset:0xa00
	s_waitcnt lgkmcnt(6)
	v_mfma_f32_32x32x16_bf16 v[64:79], v[118:121], v[134:137], v[64:79]
	ds_read_b64_tr_b16 v[134:135], v206 offset:0x1200
	ds_read_b64_tr_b16 v[136:137], v206 offset:0x1a00
	s_waitcnt lgkmcnt(6)
	v_mfma_f32_32x32x16_bf16 v[64:79], v[112:115], v[138:141], v[64:79]
	ds_read_b64_tr_b16 v[138:139], v206 offset:0x2200
	ds_read_b64_tr_b16 v[140:141], v206 offset:0x2a00
	ds_read_b64_tr_b16 v[176:177], v206 offset:0x3200
	ds_read_b64_tr_b16 v[178:179], v206 offset:0x3a00
	s_waitcnt lgkmcnt(8)
	v_mfma_f32_32x32x16_bf16 v[64:79], v[122:125], v[172:175], v[64:79]
	s_waitcnt lgkmcnt(6)
	v_mfma_f32_32x32x16_bf16 v[48:63], v[126:129], v[130:133], v[48:63]
	ds_read_b64_tr_b16 v[130:131], v206 offset:0x400
	ds_read_b64_tr_b16 v[132:133], v206 offset:0xc00
	s_waitcnt lgkmcnt(6)
	v_mfma_f32_32x32x16_bf16 v[48:63], v[118:121], v[134:137], v[48:63]
	ds_read_b64_tr_b16 v[134:135], v206 offset:0x1400
	ds_read_b64_tr_b16 v[136:137], v206 offset:0x1c00
	s_waitcnt lgkmcnt(6)
	v_mfma_f32_32x32x16_bf16 v[48:63], v[112:115], v[138:141], v[48:63]
	ds_read_b64_tr_b16 v[138:139], v206 offset:0x2400
	ds_read_b64_tr_b16 v[140:141], v206 offset:0x2c00
	ds_read_b64_tr_b16 v[172:173], v206 offset:0x3400
	ds_read_b64_tr_b16 v[174:175], v206 offset:0x3c00
	s_waitcnt lgkmcnt(8)
	v_mfma_f32_32x32x16_bf16 v[48:63], v[122:125], v[176:179], v[48:63]
	s_waitcnt lgkmcnt(6)
	v_mfma_f32_32x32x16_bf16 v[32:47], v[126:129], v[130:133], v[32:47]
	ds_read_b64_tr_b16 v[130:131], v206 offset:0x600
	ds_read_b64_tr_b16 v[132:133], v206 offset:0xe00
	s_waitcnt lgkmcnt(6)
	v_mfma_f32_32x32x16_bf16 v[32:47], v[118:121], v[134:137], v[32:47]
	ds_read_b64_tr_b16 v[134:135], v206 offset:0x1600
	ds_read_b64_tr_b16 v[136:137], v206 offset:0x1e00
	s_waitcnt lgkmcnt(6)
	v_mfma_f32_32x32x16_bf16 v[32:47], v[112:115], v[138:141], v[32:47]
	ds_read_b64_tr_b16 v[138:139], v206 offset:0x2600
	ds_read_b64_tr_b16 v[140:141], v206 offset:0x2e00
	ds_read_b64_tr_b16 v[176:177], v206 offset:0x3600
	ds_read_b64_tr_b16 v[178:179], v206 offset:0x3e00
	s_waitcnt lgkmcnt(8)
	v_mfma_f32_32x32x16_bf16 v[32:47], v[122:125], v[172:175], v[32:47]
	s_waitcnt lgkmcnt(6)
	v_mfma_f32_32x32x16_bf16 v[16:31], v[126:129], v[130:133], v[16:31]
	v_max_f32_e32 v0, v97, v97
	s_waitcnt lgkmcnt(0)
	s_barrier
	s_waitcnt vmcnt(0)
	s_waitcnt vmcnt(4)
	v_bfe_i32 v116, v217, 8, 1
	v_bfe_i32 v117, v217, 10, 1
	v_mfma_f32_32x32x16_bf16 v[16:31], v[118:121], v[134:137], v[16:31]
	v_bfe_i32 v120, v217, 1, 1
	v_bfe_i32 v121, v217, 3, 1
	v_bfe_i32 v118, v217, 12, 1
	v_bfe_i32 v126, v217, 13, 1
	v_bfe_i32 v119, v217, 14, 1
	v_bfe_i32 v127, v217, 15, 1
	s_waitcnt vmcnt(3)
	ds_write_b128 v216, v[2:5]
	s_waitcnt vmcnt(2)
	ds_write_b128 v218, v[6:9]
	s_waitcnt vmcnt(1)
	ds_write_b128 v204, v[10:13] offset:32768
	s_waitcnt vmcnt(0)
	ds_write_b128 v204, v[168:171] offset:40960
	v_mfma_f32_32x32x16_bf16 v[16:31], v[112:115], v[138:141], v[16:31]
	v_max_f32_e32 v112, v96, v96
	v_max_f32_e32 v0, v112, v0
	v_max3_f32 v0, v0, v98, v99
	v_max3_f32 v0, v0, v100, v101
	v_max3_f32 v0, v0, v102, v103
	v_max3_f32 v0, v0, v104, v105
	v_max3_f32 v0, v0, v106, v107
	v_max3_f32 v0, v0, v108, v109
	v_max3_f32 v0, v0, v110, v111
	v_max3_f32 v0, v0, v80, v81
	v_max3_f32 v0, v0, v82, v83
	v_max3_f32 v0, v0, v84, v85
	v_max3_f32 v0, v0, v86, v87
	v_max3_f32 v0, v0, v88, v89
	v_max3_f32 v0, v0, v90, v91
	v_max3_f32 v0, v0, v92, v93
	v_max3_f32 v0, v0, v94, v95
	v_mov_b32_e32 v112, v0
	s_nop 1
	v_permlane32_swap_b32_e32 v0, v112
	v_max_f32_e32 v112, v112, v112
	v_max_f32_e32 v0, v0, v0
	v_max_f32_e32 v0, v0, v112
	v_sub_f32_e32 v112, v0, v184
	v_mul_f32_e32 v112, 0x3db504f3, v112
	v_cmp_ge_f32_e32 vcc, s5, v112
	v_max_f32_e32 v112, v184, v184
	v_max_f32_e32 v128, v112, v0
	v_mfma_f32_32x32x16_bf16 v[16:31], v[122:125], v[176:179], v[16:31]
	v_sub_f32_e32 v0, v184, v128
	v_mul_f32_e32 v0, 0x3e0293ee, v0
	v_exp_f32_e32 v0, v0
	s_cmp_eq_u64 vcc, exec
	s_cselect_b64 s[2:3], -1, 0
	v_bfe_i32 v112, v217, 0, 1
	v_cndmask_b32_e64 v0, v0, 1.0, s[2:3]
	v_cmp_gt_f32_e32 vcc, 1.0, v0
	v_bfe_i32 v113, v217, 2, 1
	v_bfe_i32 v114, v217, 4, 1
	v_bfe_i32 v122, v217, 5, 1
	v_bfe_i32 v115, v217, 6, 1
	v_bfe_i32 v123, v217, 7, 1
	v_bfe_i32 v124, v217, 9, 1
	v_bfe_i32 v125, v217, 11, 1
	s_cbranch_vccz .LBB0_1816
	s_and_saveexec_b64 s[48:49], s[0:1]
	ds_write_b32 v205, v0 offset:128
	s_or_b64 exec, exec, s[48:49]
	s_waitcnt lgkmcnt(0)
	v_add_u32_e32 v129, s66, v203
	ds_read_b128 v[130:133], v129 offset:224
	ds_read_b128 v[134:137], v129 offset:192
	ds_read_b128 v[138:141], v129 offset:160
	ds_read_b128 v[172:175], v129 offset:128
	s_waitcnt lgkmcnt(3)
	v_pk_mul_f32 v[76:77], v[76:77], v[130:131]
	s_waitcnt lgkmcnt(2)
	v_pk_mul_f32 v[72:73], v[72:73], v[134:135]
	s_waitcnt lgkmcnt(1)
	v_pk_mul_f32 v[68:69], v[68:69], v[138:139]
	v_pk_mul_f32 v[78:79], v[78:79], v[132:133]
	v_pk_mul_f32 v[74:75], v[74:75], v[136:137]
	v_pk_mul_f32 v[70:71], v[70:71], v[140:141]
	s_waitcnt lgkmcnt(0)
	v_pk_mul_f32 v[66:67], v[66:67], v[174:175]
	v_pk_mul_f32 v[64:65], v[64:65], v[172:173]
	v_pk_mul_f32 v[60:61], v[60:61], v[130:131]
	v_pk_mul_f32 v[56:57], v[56:57], v[134:135]
	v_pk_mul_f32 v[52:53], v[52:53], v[138:139]
	v_pk_mul_f32 v[62:63], v[62:63], v[132:133]
	v_pk_mul_f32 v[58:59], v[58:59], v[136:137]
	v_pk_mul_f32 v[54:55], v[54:55], v[140:141]
	v_pk_mul_f32 v[50:51], v[50:51], v[174:175]
	v_pk_mul_f32 v[48:49], v[48:49], v[172:173]
	v_pk_mul_f32 v[44:45], v[44:45], v[130:131]
	v_pk_mul_f32 v[40:41], v[40:41], v[134:135]
	v_pk_mul_f32 v[36:37], v[36:37], v[138:139]
	v_pk_mul_f32 v[46:47], v[46:47], v[132:133]
	v_pk_mul_f32 v[42:43], v[42:43], v[136:137]
	v_pk_mul_f32 v[38:39], v[38:39], v[140:141]
	v_pk_mul_f32 v[34:35], v[34:35], v[174:175]
	v_pk_mul_f32 v[32:33], v[32:33], v[172:173]
	v_pk_mul_f32 v[28:29], v[28:29], v[130:131]
	v_pk_mul_f32 v[24:25], v[24:25], v[134:135]
	v_pk_mul_f32 v[20:21], v[20:21], v[138:139]
	v_pk_mul_f32 v[30:31], v[30:31], v[132:133]
	v_pk_mul_f32 v[26:27], v[26:27], v[136:137]
	v_pk_mul_f32 v[22:23], v[22:23], v[140:141]
	v_pk_mul_f32 v[18:19], v[18:19], v[174:175]
	v_pk_mul_f32 v[16:17], v[16:17], v[172:173]
